# P4 weight-converter drain loop: counted vmcnt waits so the next batch of loads stays in flight while the current one is converted
# baseline (speedup 1.0000x reference)
;     __device__ __forceinline__ CvtDesc desc(int qq) const { return cvt_desc(*F, item_of(qq), qq & 1, h); }
;     __device__ __forceinline__ void proc() { cvt_to_lds(buf, desc(q), img, gl, q & 1, h, F->lane); if (q & 1) fitem = item_of(q); ++q; }
;     __device__ __forceinline__ void flush() { if (fitem >= 0) { cvt_flush(cvt_desc(*F, fitem, 0, h), img, h, F->lane); fitem = -1; } }
;     __device__ __forceinline__ void drain() {
;         __syncthreads(); flush(); __syncthreads();
;         if (state != 0) { proc(); state = 0; if (fitem >= 0) { __syncthreads(); flush(); __syncthreads(); } }
;         if (q >= nq) { __syncthreads(); return; }
;         CvtBuf b2;
;         cvt_load(buf, desc(q), F->lane);
;         while (q < nq) {
;             if (q + 1 < nq) cvt_load(b2, desc(q + 1), F->lane);
;             cvt_to_lds(buf, desc(q), img, gl, q & 1, h, F->lane); if (q & 1) fitem = item_of(q); ++q;
;             if (fitem >= 0) { __syncthreads(); flush(); __syncthreads(); }
;             if (q >= nq) break;
;             if (q + 1 < nq) cvt_load(buf, desc(q + 1), F->lane);
;             cvt_to_lds(b2, desc(q), img, gl, q & 1, h, F->lane); if (q & 1) fitem = item_of(q); ++q;
.LBB0_904:
	s_or_b32 s0, s43, 1
	s_cmp_lt_i32 s0, s34
	s_cselect_b64 s[6:7], -1, 0
	s_lshl_b32 s44, s43, 8
	s_add_i32 s44, s44, s3
	s_cmp_ge_i32 s0, s34
	s_cbranch_scc0 .Ldr4_goA
	s_waitcnt vmcnt(0)
	s_branch .LBB0_910
.Ldr4_goA:
	s_cmpk_gt_i32 s44, 0x3fff
	s_mov_b64 s[14:15], -1
	s_cbranch_scc0 .LBB0_907
	s_add_i32 s0, s44, 0xffffc000
	s_lshr_b32 s4, s0, 8
	v_readlane_b32 s12, v254, 0
	s_lshr_b32 s36, s44, 4
	s_lshl_b64 s[0:1], s[4:5], 24
	v_readlane_b32 s14, v254, 2
	v_readlane_b32 s15, v254, 3
	s_add_u32 s0, s14, s0
	v_readlane_b32 s13, v254, 1
	v_readlane_b32 s16, v254, 4
	v_readlane_b32 s17, v254, 5
	v_readlane_b32 s18, v254, 6
	v_readlane_b32 s19, v254, 7
	s_addc_u32 s1, s15, s1
	s_mov_b64 s[14:15], 0

; #define LAS __attribute__((address_space(3)))
; __device__ __forceinline__ unsigned pk4_fp8(float a, float b, float c, float d) { int w = __builtin_amdgcn_cvt_pk_fp8_f32(a, b, 0, false); w = __builtin_amdgcn_cvt_pk_fp8_f32(c, d, w, true); return (unsigned)w; }
;     __device__ __forceinline__ CvtDesc desc(int qq) const { return cvt_desc(*F, item_of(qq), qq & 1, h); }
;     __device__ __forceinline__ void flush() { if (fitem >= 0) { cvt_flush(cvt_desc(*F, fitem, 0, h), img, h, F->lane); fitem = -1; } }
; __device__ __forceinline__ void cvt_to_lds(const CvtBuf& b, const CvtDesc& d, LAS unsigned char* img, const LAS float* gl, int sub2, int h, int lane) {
;     const int hh = lane >> 5, l5 = lane & 31;
;     float gs[16];
;     const bool use_g = d.map == 2;
; #pragma unroll
;     for (int q = 0; q < 4; ++q) { const f32x4 gv = *(const LAS f32x4*)(gl + d.k0 + 16 * hh + 4 * q);
; #pragma unroll
;         for (int j = 0; j < 4; ++j) gs[4 * q + j] = use_g ? gv[j] : WSCALE; }
;     const int c8 = 4 * h + 2 * sub2 + hh;
; #pragma unroll
;     for (int j = 0; j < 4; ++j) { u32x4 o;
; #pragma unroll
;         for (int q = 0; q < 4; ++q) { const int i = 4 * q; o[q] = pk4_fp8(b.v[i][j] * gs[i], b.v[i + 1][j] * gs[i + 1], b.v[i + 2][j] * gs[i + 2], b.v[i + 3][j] * gs[i + 3]); }
;         *(LAS u32x4*)(img + (4 * l5 + j) * 128 + 16 * (c8 ^ (l5 & 7))) = o; }
; }
;     __device__ __forceinline__ void drain() {
;     ...
;         while (q < nq) {
;             if (q + 1 < nq) cvt_load(b2, desc(q + 1), F->lane);
;             cvt_to_lds(buf, desc(q), img, gl, q & 1, h, F->lane); if (q & 1) fitem = item_of(q); ++q;
;             if (fitem >= 0) { __syncthreads(); flush(); __syncthreads(); }
;             if (q >= nq) break;
;             if (q + 1 < nq) cvt_load(buf, desc(q + 1), F->lane);
;             cvt_to_lds(b2, desc(q), img, gl, q & 1, h, F->lane); if (q & 1) fitem = item_of(q); ++q;
;             if (fitem >= 0) { __syncthreads(); flush(); __syncthreads(); }
.LBB0_910:
	s_cmpk_lt_i32 s44, 0x4000
	s_cselect_b64 s[0:1], -1, 0
	s_and_b64 s[12:13], s[0:1], exec
	s_cselect_b32 s4, 5, 4
	s_lshr_b32 s4, s44, s4
	s_lshl_b32 s4, s4, 9
	s_and_b32 s4, s4, 0x1e00
	v_add_u32_e32 v136, s4, v140
	ds_read_b128 v[154:157], v136 offset:49152
	ds_read_b128 v[158:161], v136 offset:49168
	ds_read_b128 v[162:165], v136 offset:49184
	ds_read_b128 v[166:169], v136 offset:49200
	s_andn2_b64 vcc, exec, s[6:7]
	s_waitcnt lgkmcnt(3)
	v_cndmask_b32_e64 v132, v152, v154, s[0:1]
	v_cndmask_b32_e64 v137, v152, v155, s[0:1]
	v_cndmask_b32_e64 v153, v152, v156, s[0:1]
	s_waitcnt lgkmcnt(2)
	v_cndmask_b32_e64 v171, v152, v158, s[0:1]
	v_cndmask_b32_e64 v172, v152, v159, s[0:1]
	s_waitcnt vmcnt(31)
	v_mul_f32_e32 v155, v2, v132
	s_waitcnt vmcnt(30)
	v_mul_f32_e32 v156, v6, v137
	v_mov_b32_e32 v154, v133
	v_cvt_pk_fp8_f32 v154, v155, v156
	s_waitcnt vmcnt(27)
	v_mul_f32_e32 v156, v18, v171
	s_waitcnt vmcnt(26)
	v_mul_f32_e32 v159, v22, v172
	v_mov_b32_e32 v155, v133
	v_cvt_pk_fp8_f32 v155, v156, v159
	v_cndmask_b32_e64 v170, v152, v157, s[0:1]
	v_cndmask_b32_e64 v173, v152, v160, s[0:1]
	v_cndmask_b32_e64 v174, v152, v161, s[0:1]
	v_mul_f32_e32 v157, v10, v153
	v_mul_f32_e32 v158, v14, v170
	s_waitcnt lgkmcnt(1)
	v_cndmask_b32_e64 v175, v152, v162, s[0:1]
	v_cndmask_b32_e64 v176, v152, v163, s[0:1]
	v_cvt_pk_fp8_f32 v154, v157, v158 op_sel:[0,0,1]
	s_waitcnt vmcnt(25)
	v_mul_f32_e32 v156, v26, v173
	s_waitcnt vmcnt(24)
	v_mul_f32_e32 v157, v30, v174
	s_waitcnt lgkmcnt(0)
	v_cndmask_b32_e64 v179, v152, v166, s[0:1]
	v_cndmask_b32_e64 v180, v152, v167, s[0:1]
	v_cvt_pk_fp8_f32 v155, v156, v157 op_sel:[0,0,1]
	s_waitcnt vmcnt(23)
	v_mul_f32_e32 v157, v34, v175
	s_waitcnt vmcnt(22)
	v_mul_f32_e32 v158, v38, v176
	v_mov_b32_e32 v156, v133
	v_cvt_pk_fp8_f32 v156, v157, v158
	s_waitcnt vmcnt(19)
	v_mul_f32_e32 v158, v50, v179
	s_waitcnt vmcnt(18)
	v_mul_f32_e32 v161, v54, v180
	v_mov_b32_e32 v157, v133
	v_cvt_pk_fp8_f32 v157, v158, v161
	v_cndmask_b32_e64 v177, v152, v164, s[0:1]
	v_cndmask_b32_e64 v178, v152, v165, s[0:1]
	v_cndmask_b32_e64 v181, v152, v168, s[0:1]
	v_cndmask_b32_e64 v182, v152, v169, s[0:1]
	v_mul_f32_e32 v159, v42, v177
	v_mul_f32_e32 v160, v46, v178
	v_cvt_pk_fp8_f32 v156, v159, v160 op_sel:[0,0,1]
	s_waitcnt vmcnt(17)
	v_mul_f32_e32 v158, v58, v181
	s_waitcnt vmcnt(16)
	v_mul_f32_e32 v159, v62, v182
	v_cvt_pk_fp8_f32 v157, v158, v159 op_sel:[0,0,1]
	v_mul_f32_e32 v159, v3, v132
	v_mul_f32_e32 v160, v7, v137
	v_mov_b32_e32 v158, v133
	v_cvt_pk_fp8_f32 v158, v159, v160
	v_mul_f32_e32 v160, v19, v171
	v_mul_f32_e32 v163, v23, v172
	v_mov_b32_e32 v159, v133
	v_cvt_pk_fp8_f32 v159, v160, v163
	v_mul_f32_e32 v161, v11, v153
	v_mul_f32_e32 v162, v15, v170
	v_cvt_pk_fp8_f32 v158, v161, v162 op_sel:[0,0,1]
	v_mul_f32_e32 v160, v27, v173
	v_mul_f32_e32 v161, v31, v174
	v_cvt_pk_fp8_f32 v159, v160, v161 op_sel:[0,0,1]
	v_mul_f32_e32 v161, v35, v175
	v_mul_f32_e32 v162, v39, v176
	v_mov_b32_e32 v160, v133
	v_cvt_pk_fp8_f32 v160, v161, v162
	v_mul_f32_e32 v162, v51, v179
	v_mul_f32_e32 v165, v55, v180
	v_mov_b32_e32 v161, v133
	v_cvt_pk_fp8_f32 v161, v162, v165
	v_mul_f32_e32 v163, v43, v177
	v_mul_f32_e32 v164, v47, v178
	v_cvt_pk_fp8_f32 v160, v163, v164 op_sel:[0,0,1]
	v_mul_f32_e32 v162, v59, v181
	v_mul_f32_e32 v163, v63, v182
	v_cvt_pk_fp8_f32 v161, v162, v163 op_sel:[0,0,1]
	v_mul_f32_e32 v163, v4, v132
	v_mul_f32_e32 v164, v8, v137
	v_mov_b32_e32 v162, v133
	v_cvt_pk_fp8_f32 v162, v163, v164
	v_mul_f32_e32 v164, v20, v171
	v_mul_f32_e32 v167, v24, v172
	v_mov_b32_e32 v163, v133
	v_cvt_pk_fp8_f32 v163, v164, v167
	v_mul_f32_e32 v165, v12, v153
	v_mul_f32_e32 v166, v16, v170
	v_cvt_pk_fp8_f32 v162, v165, v166 op_sel:[0,0,1]
	v_mul_f32_e32 v164, v28, v173
	v_mul_f32_e32 v165, v32, v174
	v_cvt_pk_fp8_f32 v163, v164, v165 op_sel:[0,0,1]
	v_mul_f32_e32 v165, v36, v175
	v_mul_f32_e32 v166, v40, v176
	v_mov_b32_e32 v164, v133
	v_cvt_pk_fp8_f32 v164, v165, v166
	v_mul_f32_e32 v166, v52, v179
	v_mul_f32_e32 v169, v56, v180
	v_mov_b32_e32 v165, v133
	v_cvt_pk_fp8_f32 v165, v166, v169
	v_mul_f32_e32 v167, v44, v177
	v_mul_f32_e32 v168, v48, v178
	v_cvt_pk_fp8_f32 v164, v167, v168 op_sel:[0,0,1]
	v_mul_f32_e32 v166, v60, v181
	v_mul_f32_e32 v167, v64, v182
	v_cvt_pk_fp8_f32 v165, v166, v167 op_sel:[0,0,1]
	v_mul_f32_e32 v132, v5, v132
	v_mul_f32_e32 v137, v9, v137
	v_mov_b32_e32 v166, v133
	v_cvt_pk_fp8_f32 v166, v132, v137
	v_mul_f32_e32 v132, v21, v171
	v_mul_f32_e32 v137, v25, v172
	v_mov_b32_e32 v167, v133
	v_cvt_pk_fp8_f32 v167, v132, v137
	v_mul_f32_e32 v153, v13, v153
	v_mul_f32_e32 v168, v17, v170
	v_mul_f32_e32 v132, v29, v173
	v_mul_f32_e32 v137, v33, v174
	v_cvt_pk_fp8_f32 v166, v153, v168 op_sel:[0,0,1]
	v_cvt_pk_fp8_f32 v167, v132, v137 op_sel:[0,0,1]
	v_mul_f32_e32 v132, v37, v175
	v_mul_f32_e32 v137, v41, v176
	v_mov_b32_e32 v168, v133
	v_cvt_pk_fp8_f32 v168, v132, v137
	v_mul_f32_e32 v132, v53, v179
	v_mul_f32_e32 v137, v57, v180
	v_mov_b32_e32 v169, v133
	v_cvt_pk_fp8_f32 v169, v132, v137
	v_mul_f32_e32 v153, v45, v177
	v_mul_f32_e32 v170, v49, v178
	v_mul_f32_e32 v132, v61, v181
	v_mul_f32_e32 v137, v65, v182
	v_cvt_pk_fp8_f32 v168, v153, v170 op_sel:[0,0,1]
	v_cvt_pk_fp8_f32 v169, v132, v137 op_sel:[0,0,1]
	s_mov_b64 s[6:7], -1
	ds_write_b128 v150, v[154:157]
	ds_write_b128 v150, v[158:161] offset:128
	ds_write_b128 v150, v[162:165] offset:256
	ds_write_b128 v150, v[166:169] offset:384
	s_cbranch_vccnz .LBB0_903
	s_add_i32 s43, s43, 2
	s_cmp_ge_i32 s43, s34
	s_cselect_b64 s[6:7], -1, 0
	s_and_b64 vcc, exec, s[6:7]
	s_cbranch_vccz .Ldr4_goB
	s_waitcnt vmcnt(0)
	s_branch .LBB0_917
.Ldr4_goB:
	s_lshl_b32 s46, s43, 8
	s_add_i32 s46, s46, s3
	s_cmpk_gt_i32 s46, 0x3fff
	s_mov_b64 s[36:37], -1
	s_cbranch_scc0 .LBB0_914
	s_add_i32 s4, s46, 0xffffc000
	s_lshr_b32 s4, s4, 8
	v_readlane_b32 s16, v254, 0
	s_lshr_b32 s45, s46, 4
	s_lshl_b64 s[12:13], s[4:5], 24
	v_readlane_b32 s18, v254, 2
	v_readlane_b32 s19, v254, 3
	s_add_u32 s12, s18, s12
	v_readlane_b32 s17, v254, 1
	v_readlane_b32 s20, v254, 4
	v_readlane_b32 s21, v254, 5
	v_readlane_b32 s22, v254, 6
	v_readlane_b32 s23, v254, 7
	s_addc_u32 s13, s19, s13
	s_mov_b64 s[36:37], 0

;     __device__ __forceinline__ CvtDesc desc(int qq) const { return cvt_desc(*F, item_of(qq), qq & 1, h); }
; __device__ __forceinline__ void cvt_load(CvtBuf& b, const CvtDesc& d, int lane) {
;     const float* p = d.W + (size_t)(d.k0 + 16 * (lane >> 5)) * d.ldw + d.n0 + 4 * (lane & 31);
; #pragma unroll
;     for (int i = 0; i < 16; ++i) b.v[i] = __builtin_nontemporal_load((const f32x4*)(p + (size_t)i * d.ldw));
; }
;     __device__ __forceinline__ void drain() {
;     ...
;             if (q + 1 < nq) cvt_load(buf, desc(q + 1), F->lane);
;             cvt_to_lds(b2, desc(q), img, gl, q & 1, h, F->lane); if (q & 1) fitem = item_of(q); ++q;
.LBB0_916:
	s_lshl_b32 s15, s45, 7
	s_and_b32 s15, s15, 0x780
	v_or_b32_e32 v2, s15, v131
	v_mul_u32_u24_e32 v2, s14, v2
	v_lshlrev_b32_e32 v132, 2, v2
	s_lshl_b32 s4, s4, 7
	v_lshl_add_u64 v[2:3], s[12:13], 0, v[132:133]
	v_lshl_add_u64 v[2:3], s[4:5], 2, v[2:3]
	v_lshlrev_b32_e32 v132, 2, v130
	v_lshl_add_u64 v[10:11], v[2:3], 0, v[132:133]
	s_lshl_b32 s4, s14, 2
	v_lshl_add_u64 v[12:13], v[10:11], 0, s[4:5]
	v_lshl_add_u64 v[18:19], v[12:13], 0, s[4:5]
	v_lshl_add_u64 v[20:21], v[18:19], 0, s[4:5]
	v_lshl_add_u64 v[26:27], v[20:21], 0, s[4:5]
	v_lshl_add_u64 v[28:29], v[26:27], 0, s[4:5]
	v_lshl_add_u64 v[34:35], v[28:29], 0, s[4:5]
	v_lshl_add_u64 v[36:37], v[34:35], 0, s[4:5]
	v_lshl_add_u64 v[38:39], v[36:37], 0, s[4:5]
	v_lshl_add_u64 v[42:43], v[38:39], 0, s[4:5]
	v_lshl_add_u64 v[46:47], v[42:43], 0, s[4:5]
	v_lshl_add_u64 v[50:51], v[46:47], 0, s[4:5]
	v_lshl_add_u64 v[54:55], v[50:51], 0, s[4:5]
	v_lshl_add_u64 v[58:59], v[54:55], 0, s[4:5]
	v_lshl_add_u64 v[62:63], v[58:59], 0, s[4:5]
	global_load_dwordx4 v[2:5], v[10:11], off nt
	global_load_dwordx4 v[6:9], v[12:13], off nt
	s_nop 0
	global_load_dwordx4 v[10:13], v[18:19], off nt
	global_load_dwordx4 v[14:17], v[20:21], off nt
	s_nop 0
	global_load_dwordx4 v[18:21], v[26:27], off nt
	global_load_dwordx4 v[22:25], v[28:29], off nt
	s_nop 0
	global_load_dwordx4 v[26:29], v[34:35], off nt
	global_load_dwordx4 v[30:33], v[36:37], off nt
	s_nop 0
	global_load_dwordx4 v[34:37], v[38:39], off nt
	s_nop 0
	global_load_dwordx4 v[38:41], v[42:43], off nt
	s_nop 0
	global_load_dwordx4 v[42:45], v[46:47], off nt
	s_nop 0
	global_load_dwordx4 v[46:49], v[50:51], off nt
	s_nop 0
	global_load_dwordx4 v[50:53], v[54:55], off nt
	s_nop 0
	global_load_dwordx4 v[54:57], v[58:59], off nt
	s_nop 0
	global_load_dwordx4 v[58:61], v[62:63], off nt
	v_lshl_add_u64 v[62:63], v[62:63], 0, s[4:5]
	global_load_dwordx4 v[62:65], v[62:63], off nt
	s_waitcnt vmcnt(16)
